# sparse attention: 31 address VALU per query hoisted or folded into offsets; on top of indexer interleave and stick-breaking load hoist
# baseline (speedup 1.0000x reference)
.LBB0_802:
	s_or_b64 exec, exec, s[4:5]
	v_lshlrev_b32_e32 v11, 2, v90
	v_bfe_u32 v14, v90, 2, 2
	v_and_b32_e32 v11, 12, v11
	v_bitop3_b32 v12, v11, v2, v14 bitop3:0x36
	v_lshlrev_b32_e32 v93, 4, v12
	v_add_u32_e32 v12, 2, v2
	v_bitop3_b32 v12, v11, v12, v14 bitop3:0x36
	v_lshlrev_b32_e32 v94, 4, v12
	v_add_u32_e32 v12, 4, v2
	v_bitop3_b32 v12, v11, v12, v14 bitop3:0x36
	v_lshlrev_b32_e32 v95, 4, v12
	v_add_u32_e32 v12, 6, v2
	v_bitop3_b32 v12, v11, v12, v14 bitop3:0x36
	v_lshlrev_b32_e32 v96, 4, v12
	v_add_u32_e32 v12, 8, v2
	v_bitop3_b32 v12, v11, v12, v14 bitop3:0x36
	v_readlane_b32 s4, v252, 60
	v_lshlrev_b32_e32 v97, 4, v12
	v_add_u32_e32 v12, 10, v2
	s_waitcnt lgkmcnt(0)
	s_mov_b32 s6, s4
	v_bitop3_b32 v12, v11, v12, v14 bitop3:0x36
	v_add_lshl_u32 v9, v2, s6, 8
	v_lshlrev_b32_e32 v1, 6, v2
	v_lshlrev_b32_e32 v98, 4, v12
	v_add_u32_e32 v12, 12, v2
	v_add_u32_e32 v2, 14, v2
	v_bitop3_b32 v2, v11, v2, v14 bitop3:0x36
	v_lshlrev_b32_e32 v100, 4, v2
	v_lshrrev_b32_e32 v2, 3, v90
	s_movk_i32 s4, 0xf0
	v_bitop3_b32 v12, v11, v12, v14 bitop3:0x36
	v_and_b32_e32 v15, 0x1ffffffc, v2
	v_bitop3_b32 v92, v1, v4, s4 bitop3:0x78
	v_lshlrev_b32_e32 v99, 4, v12
	v_add_u32_e32 v12, 8, v15
	v_and_b32_e32 v2, 2, v2
	v_bfe_u32 v81, v90, 1, 1
	v_readlane_b32 s4, v253, 16
	v_bfe_u32 v11, v12, 2, 2
	v_lshlrev_b32_e32 v80, 2, v14
	v_or3_b32 v81, v2, s4, v81
	v_bitop3_b32 v2, v11, v81, v80 bitop3:0x36
	v_lshlrev_b32_e32 v11, 4, v2
	v_or_b32_e32 v2, v12, v14
	v_lshlrev_b32_e32 v12, 8, v2
	v_and_b32_e32 v2, 8, v13
	v_bfe_u32 v13, v90, 5, 2
	v_or_b32_e32 v14, v15, v14
	v_ashrrev_i32_e32 v15, 3, v90
	v_readlane_b32 s4, v253, 18
	v_bitop3_b32 v13, v80, v81, v13 bitop3:0x36
	v_readlane_b32 s5, v252, 61
	v_add_u32_e32 v80, s4, v15
	v_lshlrev_b32_e32 v81, 9, v80
	v_readlane_b32 s4, v253, 14
	v_and_b32_e32 v88, 0xfffffc00, v81
	v_lshlrev_b32_e32 v15, 5, v15
	v_and_or_b32 v81, v90, 7, s4
	v_lshl_add_u32 v84, v81, 5, v80
	v_add_u32_e32 v80, 0x100, v84
	v_readlane_b32 s4, v253, 19
	v_and_or_b32 v15, v15, 32, v81
	v_ashrrev_i32_e32 v81, 31, v80
	v_readlane_b32 s5, v253, 20
	v_ashrrev_i32_e32 v85, 31, v84
	v_lshlrev_b32_e32 v0, 12, v90
	v_lshl_add_u64 v[80:81], v[80:81], 4, s[4:5]
	v_lshl_add_u64 v[84:85], v[84:85], 4, s[4:5]
	global_load_dwordx4 v[80:83], v[80:81], off
	s_add_i32 s4, 0, 0x20000
	global_load_dwordx4 v[84:87], v[84:85], off
	v_and_b32_e32 v0, 0x10000, v0
	v_and_or_b32 v10, v90, 31, s6
	v_lshlrev_b32_e32 v13, 4, v13
	v_lshlrev_b32_e32 v14, 8, v14
	v_lshl_add_u32 v15, v15, 4, s4
	v_readlane_b32 s4, v253, 23
	v_xor_b32_e32 v1, 0x80, v92
	v_xor_b32_e32 v3, 16, v92
	v_xor_b32_e32 v4, 0x90, v92
	v_xor_b32_e32 v5, 32, v92
	v_xor_b32_e32 v6, 0xa0, v92
	v_xor_b32_e32 v7, 48, v92
	v_xor_b32_e32 v8, 0xb0, v92
	v_add3_u32 v13, s4, v13, v14
	v_add3_u32 v11, s4, v11, v12
	v_add3_u32 v101, 0, v9, v0
	v_lshl_add_u32 v102, v10, 8, 0
	v_readlane_b32 s4, v255, 10
	v_readlane_b32 s6, v254, 56
	v_add_u32_e32 v103, 0x10000, v102
	s_mov_b32 s14, 0
	v_add_u32_e32 v104, v101, v1
	v_add_u32_e32 v105, v101, v3
	v_add_u32_e32 v106, v101, v4
	v_add_u32_e32 v107, v101, v5
	v_add_u32_e32 v108, v101, v6
	v_add_u32_e32 v109, v101, v7
	v_add_u32_e32 v110, v101, v8
	v_add_u32_e32 v111, v15, v88
	v_add_u32_e32 v112, v13, v2
	v_add_u32_e32 v113, v11, v2
	v_readlane_b32 s5, v255, 11
	s_mov_b32 s16, s6
	v_readlane_b32 s7, v254, 57
	v_add_u32_e32 v226, v102, v93
	v_add_u32_e32 v227, v102, v94
	v_add_u32_e32 v228, v102, v95
	v_add_u32_e32 v229, v102, v96
	v_add_u32_e32 v230, v102, v97
	v_add_u32_e32 v231, v102, v98
	v_add_u32_e32 v232, v102, v99
	v_add_u32_e32 v233, v102, v100
	v_add_u32_e32 v234, v103, v93
	v_add_u32_e32 v235, v103, v94
	v_add_u32_e32 v236, v103, v95
	v_add_u32_e32 v237, v103, v96
	v_add_u32_e32 v238, v103, v97
	v_add_u32_e32 v239, v103, v98
	v_add_u32_e32 v240, v103, v99
	v_add_u32_e32 v241, v103, v100
	s_branch .LBB0_804

.LBB0_804:
	v_mov_b32_e32 v89, v90
	s_add_i32 s15, s16, s28
	s_and_b32 s17, s14, 1
	s_waitcnt lgkmcnt(0)
	s_barrier
	v_add_u32_e32 v0, v101, v92
	s_cmpk_gt_i32 s15, 0x7fff
	v_lshlrev_b32_e32 v88, 4, v89
	s_waitcnt vmcnt(33)
	ds_write_b128 v0, v[16:19]
	s_waitcnt vmcnt(32)
	ds_write_b128 v104, v[20:23] offset:512
	s_waitcnt vmcnt(31)
	ds_write_b128 v105, v[24:27] offset:1024
	s_waitcnt vmcnt(30)
	ds_write_b128 v106, v[28:31] offset:1536
	s_waitcnt vmcnt(29)
	ds_write_b128 v107, v[32:35] offset:2048
	s_waitcnt vmcnt(28)
	ds_write_b128 v108, v[36:39] offset:2560
	s_waitcnt vmcnt(27)
	ds_write_b128 v109, v[40:43] offset:3072
	s_waitcnt vmcnt(26)
	ds_write_b128 v110, v[44:47] offset:3584
	s_waitcnt vmcnt(25)
	ds_write_b128 v0, v[48:51] offset:4096
	s_waitcnt vmcnt(24)
	ds_write_b128 v104, v[52:55] offset:4608
	s_waitcnt vmcnt(23)
	ds_write_b128 v105, v[56:59] offset:5120
	s_waitcnt vmcnt(22)
	ds_write_b128 v106, v[60:63] offset:5632
	s_waitcnt vmcnt(21)
	ds_write_b128 v107, v[64:67] offset:6144
	s_waitcnt vmcnt(20)
	ds_write_b128 v108, v[68:71] offset:6656
	s_waitcnt vmcnt(19)
	ds_write_b128 v109, v[72:75] offset:7168
	s_waitcnt vmcnt(18)
	ds_write_b128 v110, v[76:79] offset:7680
	s_waitcnt vmcnt(0)
	ds_write_b128 v111, v[84:87]
	ds_write_b128 v111, v[80:83] offset:128
	s_cselect_b64 s[6:7], -1, 0
	s_cmp_lt_i32 s15, 0x8000
	v_add_u32_e32 v0, 0, v88
	s_waitcnt lgkmcnt(0)
	s_barrier
	s_cselect_b32 s8, s15, s16
	v_add_u32_e32 v77, 0x20000, v0
	s_ashr_i32 s9, s8, 31
	ds_read_b128 v[0:3], v226
	ds_read_b128 v[4:7], v77
	s_lshr_b32 s10, s9, 20
	s_add_i32 s10, s8, s10
	s_ashr_i32 s10, s10, 12
	s_ashr_i32 s11, s10, 31
	s_lshl_b64 s[12:13], s[10:11], 21
	v_readlane_b32 s11, v253, 2
	v_and_b32_e32 v130, 31, v89
	s_waitcnt lgkmcnt(0)
	v_mfma_f32_32x32x16_bf16 v[0:15], v[0:3], v[4:7], 0
	s_add_u32 s12, s11, s12
	v_readlane_b32 s11, v253, 3
	v_lshlrev_b32_e32 v76, 4, v130
	s_addc_u32 s13, s11, s13
	v_lshl_or_b32 v16, v121, 9, v76
	global_load_dwordx4 v[16:19], v16, s[12:13]
	ds_read_b128 v[20:23], v227
	ds_read_b128 v[24:27], v77 offset:1024
	s_waitcnt lgkmcnt(0)
	v_mfma_f32_32x32x16_bf16 v[0:15], v[20:23], v[24:27], v[0:15]
	v_lshl_or_b32 v20, v123, 9, v76
	global_load_dwordx4 v[20:23], v20, s[12:13]
	ds_read_b128 v[24:27], v228
	ds_read_b128 v[28:31], v77 offset:2048
	v_add_u32_e32 v80, s44, v89
	s_movk_i32 s11, 0x100
	s_waitcnt lgkmcnt(0)
	v_mfma_f32_32x32x16_bf16 v[0:15], v[24:27], v[28:31], v[0:15]
	v_lshl_or_b32 v24, v116, 9, v76
	global_load_dwordx4 v[24:27], v24, s[12:13]
	ds_read_b128 v[28:31], v229
	ds_read_b128 v[32:35], v77 offset:3072
	v_cmp_gt_i32_e32 vcc, s11, v80
	s_waitcnt lgkmcnt(0)
	v_mfma_f32_32x32x16_bf16 v[0:15], v[28:31], v[32:35], v[0:15]
	v_lshl_or_b32 v28, v124, 9, v76
	global_load_dwordx4 v[28:31], v28, s[12:13]
	ds_read_b128 v[32:35], v230
	ds_read_b128 v[36:39], v77 offset:4096
	s_waitcnt lgkmcnt(0)
	v_mfma_f32_32x32x16_bf16 v[0:15], v[32:35], v[36:39], v[0:15]
	v_lshl_or_b32 v32, v119, 9, v76
	global_load_dwordx4 v[32:35], v32, s[12:13]
	ds_read_b128 v[36:39], v231
	ds_read_b128 v[40:43], v77 offset:5120
	s_waitcnt lgkmcnt(0)
	v_mfma_f32_32x32x16_bf16 v[0:15], v[36:39], v[40:43], v[0:15]
	v_lshl_or_b32 v36, v120, 9, v76
	global_load_dwordx4 v[36:39], v36, s[12:13]
	ds_read_b128 v[40:43], v232
	ds_read_b128 v[44:47], v77 offset:6144
	s_waitcnt lgkmcnt(0)
	v_mfma_f32_32x32x16_bf16 v[0:15], v[40:43], v[44:47], v[0:15]
	v_lshl_or_b32 v40, v117, 9, v76
	global_load_dwordx4 v[40:43], v40, s[12:13]
	ds_read_b128 v[44:47], v233
	ds_read_b128 v[48:51], v77 offset:7168
	s_waitcnt lgkmcnt(0)
	v_mfma_f32_32x32x16_bf16 v[0:15], v[44:47], v[48:51], v[0:15]
	v_lshl_or_b32 v44, v125, 9, v76
	global_load_dwordx4 v[44:47], v44, s[12:13]
	ds_read_b128 v[48:51], v234
	ds_read_b128 v[52:55], v77 offset:8192
	s_waitcnt lgkmcnt(0)
	v_mfma_f32_32x32x16_bf16 v[0:15], v[48:51], v[52:55], v[0:15]
	v_lshl_or_b32 v48, v118, 9, v76
	global_load_dwordx4 v[48:51], v48, s[12:13]
	ds_read_b128 v[52:55], v235
	ds_read_b128 v[56:59], v77 offset:9216
	s_waitcnt lgkmcnt(0)
	v_mfma_f32_32x32x16_bf16 v[0:15], v[52:55], v[56:59], v[0:15]
	v_lshl_or_b32 v52, v114, 9, v76
	global_load_dwordx4 v[52:55], v52, s[12:13]
	ds_read_b128 v[56:59], v236
	ds_read_b128 v[60:63], v77 offset:10240
	s_waitcnt lgkmcnt(0)
	v_mfma_f32_32x32x16_bf16 v[0:15], v[56:59], v[60:63], v[0:15]
	v_lshl_or_b32 v56, v115, 9, v76
	global_load_dwordx4 v[56:59], v56, s[12:13]
	ds_read_b128 v[60:63], v237
	ds_read_b128 v[64:67], v77 offset:11264
	s_waitcnt lgkmcnt(0)
	v_mfma_f32_32x32x16_bf16 v[0:15], v[60:63], v[64:67], v[0:15]
	v_lshl_or_b32 v60, v122, 9, v76
	global_load_dwordx4 v[60:63], v60, s[12:13]
	ds_read_b128 v[64:67], v238
	ds_read_b128 v[68:71], v77 offset:12288
	s_waitcnt lgkmcnt(0)
	v_mfma_f32_32x32x16_bf16 v[0:15], v[64:67], v[68:71], v[0:15]
	v_lshl_or_b32 v64, v126, 9, v76
	global_load_dwordx4 v[64:67], v64, s[12:13]
	ds_read_b128 v[68:71], v239
	ds_read_b128 v[72:75], v77 offset:13312
	s_waitcnt lgkmcnt(0)
	v_mfma_f32_32x32x16_bf16 v[0:15], v[68:71], v[72:75], v[0:15]
	v_lshl_or_b32 v68, v127, 9, v76
	global_load_dwordx4 v[68:71], v68, s[12:13]
	ds_read_b128 v[72:75], v240
	ds_read_b128 v[82:85], v77 offset:14336
	s_waitcnt lgkmcnt(0)
	v_mfma_f32_32x32x16_bf16 v[0:15], v[72:75], v[82:85], v[0:15]
	v_lshl_or_b32 v72, v128, 9, v76
	v_lshl_or_b32 v76, v129, 9, v76
	global_load_dwordx4 v[72:75], v72, s[12:13]
	ds_read_b128 v[82:85], v241
	ds_read_b128 v[114:117], v77 offset:15360
	global_load_dwordx4 v[76:79], v76, s[12:13]
	s_waitcnt lgkmcnt(0)
	v_mfma_f32_32x32x16_bf16 v[0:15], v[82:85], v[114:117], v[0:15]
	s_and_saveexec_b64 s[12:13], vcc
	s_cbranch_execz .LBB0_808
	s_lshl_b32 s10, s10, 12
	s_sub_i32 s18, s8, s10
	v_cmp_ge_i32_e32 vcc, s18, v80
	v_mov_b32_e32 v81, 0x1000
	s_and_saveexec_b64 s[10:11], vcc
	s_cbranch_execz .LBB0_807
	v_sub_u32_e32 v81, s18, v91
	v_mov_b32_e32 v82, 0x7f
	v_med3_i32 v81, v81, 0, v82
	v_add_u32_e32 v81, 0, v81
	v_add_u32_e32 v81, 0x25e80, v81
	ds_read_u8 v81, v81
	s_waitcnt lgkmcnt(0)
	v_lshlrev_b32_e32 v81, 7, v81

.LBB0_808:
	s_or_b64 exec, exec, s[12:13]
	v_readlane_b32 s10, v253, 24
	v_readlane_b32 s11, v253, 14
	s_add_i32 s10, s10, s16
	s_lshl_b64 s[8:9], s[8:9], 14
	v_and_or_b32 v80, v89, 7, s11
	v_lshrrev_b32_e32 v81, 3, v89
	v_readlane_b32 s11, v253, 18
	s_add_u32 s8, s50, s8
	s_addc_u32 s9, s51, s9
	v_add_lshl_u32 v81, v81, s11, 4
	v_lshl_add_u32 v80, v80, 9, v81
	global_load_dwordx4 v[84:87], v80, s[8:9]
	v_add_u32_e32 v80, 0x1000, v80
	v_ashrrev_i32_e32 v114, 3, v89
	global_load_dwordx4 v[80:83], v80, s[8:9]
	s_lshl_b32 s8, s17, 10
	v_readlane_b32 s9, v253, 15
	v_lshlrev_b32_e32 v114, 2, v114
	s_add_i32 s8, s9, s8
	v_and_b32_e32 v114, -16, v114
	v_add_u32_e32 v122, s8, v114
	ds_read_b128 v[114:117], v122
	ds_read_b128 v[118:121], v122 offset:32
	s_add_i32 s8, 0, 0x24a00
	v_lshl_add_u32 v123, v130, 2, s8
	s_mov_b32 s8, 0xff800000
	s_waitcnt lgkmcnt(1)
	v_add_u32_e32 v124, v123, v114
	v_add_u32_e32 v125, v123, v115
	v_add_u32_e32 v126, v123, v116
	v_add_u32_e32 v127, v123, v117
	ds_read_b128 v[114:117], v122 offset:64
	s_waitcnt lgkmcnt(1)
	v_add_u32_e32 v118, v123, v118
	v_add_u32_e32 v119, v123, v119
	v_add_u32_e32 v120, v123, v120
	v_add_u32_e32 v121, v123, v121
	s_waitcnt lgkmcnt(0)
	v_add_u32_e32 v128, v123, v114
	v_add_u32_e32 v129, v123, v115
	v_add_u32_e32 v131, v123, v116
	v_add_u32_e32 v132, v123, v117
	ds_read_b128 v[114:117], v122 offset:96
	v_readlane_b32 s9, v255, 14
	s_cmp_lt_i32 s10, 0x8000
	s_waitcnt lgkmcnt(0)
	v_add_u32_e32 v114, v123, v114
	v_add_u32_e32 v115, v123, v115
	v_add_u32_e32 v116, v123, v116
	v_add_u32_e32 v117, v123, v117
	ds_read_b32 v117, v117
	ds_read_b32 v116, v116
	ds_read_b32 v115, v115
	ds_read_b32 v114, v114
	ds_read_b32 v122, v132
	ds_read_b32 v123, v131
	ds_read_b32 v129, v129
	ds_read_b32 v128, v128
	ds_read_b32 v121, v121
	ds_read_b32 v120, v120
	ds_read_b32 v119, v119
	ds_read_b32 v118, v118
	ds_read_b32 v127, v127
	ds_read_b32 v126, v126
	ds_read_b32 v125, v125
	ds_read_b32 v124, v124
	s_waitcnt lgkmcnt(0)
	s_waitcnt lgkmcnt(0)
	s_nop 0
	v_fmac_f32_e32 v124, 0x3e0293ee, v0
	v_fmac_f32_e32 v125, 0x3e0293ee, v1
	v_max3_f32 v0, v124, s8, v125
	v_fmac_f32_e32 v126, 0x3e0293ee, v2
	v_fmac_f32_e32 v127, 0x3e0293ee, v3
	v_max3_f32 v0, v0, v126, v127
	v_fmac_f32_e32 v118, 0x3e0293ee, v4
	v_fmac_f32_e32 v119, 0x3e0293ee, v5
	v_max3_f32 v0, v0, v118, v119
	v_fmac_f32_e32 v120, 0x3e0293ee, v6
	v_fmac_f32_e32 v121, 0x3e0293ee, v7
	v_max3_f32 v0, v0, v120, v121
	v_fmac_f32_e32 v128, 0x3e0293ee, v8
	v_fmac_f32_e32 v129, 0x3e0293ee, v9
	v_max3_f32 v0, v0, v128, v129
	v_fmac_f32_e32 v123, 0x3e0293ee, v10
	v_fmac_f32_e32 v122, 0x3e0293ee, v11
	v_max3_f32 v0, v0, v123, v122
	v_fmac_f32_e32 v114, 0x3e0293ee, v12
	v_fmac_f32_e32 v115, 0x3e0293ee, v13
	v_max3_f32 v0, v0, v114, v115
	v_fmac_f32_e32 v116, 0x3e0293ee, v14
	v_fmac_f32_e32 v117, 0x3e0293ee, v15
	v_max3_f32 v0, v0, v116, v117
	v_mov_b32_e32 v1, v0
	v_mov_b32_e32 v2, v0
	v_and_b32_e32 v3, 32, v89
	s_nop 0
	v_permlane32_swap_b32_e32 v1, v2
	v_cmp_eq_u32_e32 vcc, 0, v3
	v_readlane_b32 s8, v252, 8
	s_nop 0
	v_cndmask_b32_e32 v1, v1, v2, vcc
	v_max_f32_e32 v1, v1, v1
	v_max_f32_e32 v0, v0, v1
	v_lshlrev_b32_e32 v1, 3, v130
	v_add_lshl_u32 v8, v1, s8, 2
	v_readlane_b32 s8, v255, 13
	s_nop 1
	v_add_u32_e32 v1, s8, v8
	ds_write_b32 v1, v0
	s_waitcnt lgkmcnt(0)
	s_barrier
	v_lshl_add_u32 v4, v130, 5, s8
	ds_read_b128 v[0:3], v4
	ds_read_b128 v[4:7], v4 offset:16
	v_add_u32_e32 v8, s9, v8
	v_readlane_b32 s8, v253, 21
	s_waitcnt lgkmcnt(1)
	v_max_f32_e32 v1, v1, v1
	v_max_f32_e32 v0, v0, v0
	v_max_f32_e32 v0, v0, v1
	v_max_f32_e32 v1, v3, v3
	v_max_f32_e32 v2, v2, v2
	v_max_f32_e32 v1, v2, v1
	s_waitcnt lgkmcnt(0)
	v_max_f32_e32 v2, v7, v7
	v_max_f32_e32 v3, v6, v6
	v_max_f32_e32 v2, v3, v2
	v_max3_f32 v2, v4, v5, v2
	v_max3_f32 v0, v0, v1, v2
	v_sub_f32_e32 v1, v124, v0
	v_sub_f32_e32 v2, v125, v0
	v_sub_f32_e32 v3, v126, v0
	v_sub_f32_e32 v4, v127, v0
	v_exp_f32_e32 v1, v1
	v_exp_f32_e32 v2, v2
	v_exp_f32_e32 v3, v3
	v_exp_f32_e32 v4, v4
	v_sub_f32_e32 v5, v118, v0
	v_sub_f32_e32 v6, v119, v0
	v_sub_f32_e32 v7, v120, v0
	v_sub_f32_e32 v9, v121, v0
	v_exp_f32_e32 v5, v5
	v_exp_f32_e32 v6, v6
	v_exp_f32_e32 v7, v7
	v_exp_f32_e32 v9, v9
	v_sub_f32_e32 v10, v128, v0
	v_sub_f32_e32 v11, v129, v0
	v_sub_f32_e32 v12, v123, v0
	v_sub_f32_e32 v13, v122, v0
	v_exp_f32_e32 v10, v10
	v_exp_f32_e32 v11, v11
	v_exp_f32_e32 v12, v12
	v_exp_f32_e32 v13, v13
	v_sub_f32_e32 v14, v114, v0
	v_sub_f32_e32 v15, v115, v0
	v_sub_f32_e32 v89, v116, v0
	v_sub_f32_e32 v0, v117, v0
	v_exp_f32_e32 v14, v14
	v_exp_f32_e32 v15, v15
	v_exp_f32_e32 v89, v89
	v_exp_f32_e32 v114, v0
	v_add_f32_e32 v0, v1, v2
	v_add_f32_e32 v115, v3, v4
	v_add_f32_e32 v0, v0, v115
	v_add_f32_e32 v115, v5, v6
	v_add_f32_e32 v116, v7, v9
	v_add_f32_e32 v115, v115, v116
	v_add_f32_e32 v0, v0, v115
	v_add_f32_e32 v115, v10, v11
	v_add_f32_e32 v116, v12, v13
	v_add_f32_e32 v115, v115, v116
	v_add_f32_e32 v116, v14, v15
	v_add_f32_e32 v117, v89, v114
	v_add_f32_e32 v116, v116, v117
	v_add_f32_e32 v115, v115, v116
	v_add_f32_e32 v0, v0, v115
	v_mov_b32_e32 v115, v0
	v_mov_b32_e32 v116, v0
	s_nop 1
	v_permlane32_swap_b32_e32 v115, v116
	v_cndmask_b32_e32 v115, v115, v116, vcc
	v_add_f32_e32 v0, v0, v115
	ds_write_b32 v8, v0
	v_add_u32_e32 v8, s8, v88
	v_cvt_pk_bf16_f32 v0, v1, v2
	v_cvt_pk_bf16_f32 v1, v3, v4
	v_cvt_pk_bf16_f32 v2, v5, v6
	v_cvt_pk_bf16_f32 v3, v7, v9
	ds_write_b128 v8, v[0:3]
	v_cvt_pk_bf16_f32 v0, v10, v11
	v_cvt_pk_bf16_f32 v1, v12, v13
	v_cvt_pk_bf16_f32 v2, v14, v15
	v_cvt_pk_bf16_f32 v3, v89, v114
	ds_write_b128 v8, v[0:3] offset:1024
	v_mov_b32_e32 v89, v90
	s_waitcnt lgkmcnt(0)
	s_barrier
	v_readlane_b32 s8, v253, 22
	v_and_b32_e32 v130, 31, v89
	v_lshl_add_u32 v4, v130, 5, s9
	ds_read_b128 v[0:3], v4
	ds_read_b128 v[4:7], v4 offset:16
	v_add_u32_e32 v131, s44, v89
	s_waitcnt lgkmcnt(1)
	v_add_f32_e32 v0, v0, v1
	v_add_f32_e32 v1, v2, v3
	v_add_f32_e32 v0, v0, v1
	s_waitcnt lgkmcnt(0)
	v_add_f32_e32 v1, v4, v5
	v_add_f32_e32 v2, v6, v7
	v_add_f32_e32 v1, v1, v2
	v_add_f32_e32 v0, v0, v1
	v_rcp_f32_e32 v0, v0
	v_lshl_add_u32 v1, v130, 2, s8
	s_cselect_b32 s8, s10, s16
	s_ashr_i32 s9, s8, 31
	ds_write_b32 v1, v0
	v_ashrrev_i32_e32 v0, 3, v89
	v_and_b32_e32 v88, -4, v0
	v_lshl_add_u32 v0, v89, 4, 0
	v_add_u32_e32 v129, 0x20000, v0
	ds_read_b128 v[0:3], v129
	ds_read_b64_tr_b16 v[4:5], v112
	ds_read_b64_tr_b16 v[6:7], v113
	s_lshl_b64 s[8:9], s[8:9], 10
	v_readlane_b32 s10, v253, 6
	s_add_u32 s10, s10, s8
	v_readlane_b32 s8, v253, 7
	s_addc_u32 s11, s8, s9
	v_readlane_b32 s8, v253, 8
	s_waitcnt lgkmcnt(0)
	v_mfma_f32_32x32x16_bf16 v[0:15], v[0:3], v[4:7], 0
	v_readlane_b32 s9, v253, 9
	s_add_u32 s8, s10, s8
	s_addc_u32 s9, s11, s9
	s_nop 1
	global_load_dword v121, v88, s[8:9]
	ds_read_b128 v[114:117], v129 offset:1024
	ds_read_b64_tr_b16 v[122:123], v112 offset:4096
	ds_read_b64_tr_b16 v[124:125], v113 offset:4096
	s_waitcnt lgkmcnt(0)
	v_mfma_f32_32x32x16_bf16 v[0:15], v[114:117], v[122:125], v[0:15]
	global_load_dword v123, v88, s[8:9] offset:8
	ds_read_b128 v[114:117], v129 offset:2048
	ds_read_b64_tr_b16 v[124:125], v112 offset:8192
	ds_read_b64_tr_b16 v[126:127], v113 offset:8192
	s_waitcnt lgkmcnt(0)
	v_mfma_f32_32x32x16_bf16 v[0:15], v[114:117], v[124:127], v[0:15]
	global_load_dword v116, v88, s[8:9] offset:16
	ds_read_b128 v[124:127], v129 offset:3072
	ds_read_b64_tr_b16 v[132:133], v112 offset:12288
	ds_read_b64_tr_b16 v[134:135], v113 offset:12288
	s_waitcnt lgkmcnt(0)
	v_mfma_f32_32x32x16_bf16 v[0:15], v[124:127], v[132:135], v[0:15]
	global_load_dword v124, v88, s[8:9] offset:24
	ds_read_b128 v[132:135], v129 offset:4096
	ds_read_b64_tr_b16 v[136:137], v112 offset:16384
	ds_read_b64_tr_b16 v[138:139], v113 offset:16384
	global_load_dword v119, v88, s[8:9] offset:32
	s_waitcnt lgkmcnt(0)
	v_mfma_f32_32x32x16_bf16 v[0:15], v[132:135], v[136:139], v[0:15]
	ds_read_b128 v[132:135], v129 offset:5120
	ds_read_b64_tr_b16 v[136:137], v112 offset:20480
	ds_read_b64_tr_b16 v[138:139], v113 offset:20480
	global_load_dword v120, v88, s[8:9] offset:40
	s_waitcnt lgkmcnt(0)
	v_mfma_f32_32x32x16_bf16 v[0:15], v[132:135], v[136:139], v[0:15]
	ds_read_b128 v[132:135], v129 offset:6144
	ds_read_b64_tr_b16 v[136:137], v112 offset:24576
	ds_read_b64_tr_b16 v[138:139], v113 offset:24576
	global_load_dword v117, v88, s[8:9] offset:48
	s_waitcnt lgkmcnt(0)
	v_mfma_f32_32x32x16_bf16 v[0:15], v[132:135], v[136:139], v[0:15]
	ds_read_b128 v[132:135], v129 offset:7168
	ds_read_b64_tr_b16 v[136:137], v112 offset:28672
	ds_read_b64_tr_b16 v[138:139], v113 offset:28672
	global_load_dword v125, v88, s[8:9] offset:56
	s_waitcnt lgkmcnt(0)
	v_mfma_f32_32x32x16_bf16 v[0:15], v[132:135], v[136:139], v[0:15]
	ds_read_b128 v[132:135], v129 offset:8192
	ds_read_b64_tr_b16 v[136:137], v112 offset:32768
	ds_read_b64_tr_b16 v[138:139], v113 offset:32768
	global_load_dword v118, v88, s[8:9] offset:64
	s_waitcnt lgkmcnt(0)
	v_mfma_f32_32x32x16_bf16 v[0:15], v[132:135], v[136:139], v[0:15]
	ds_read_b128 v[132:135], v129 offset:9216
	ds_read_b64_tr_b16 v[136:137], v112 offset:36864
	ds_read_b64_tr_b16 v[138:139], v113 offset:36864
	global_load_dword v114, v88, s[8:9] offset:72
	s_waitcnt lgkmcnt(0)
	v_mfma_f32_32x32x16_bf16 v[0:15], v[132:135], v[136:139], v[0:15]
	ds_read_b128 v[132:135], v129 offset:10240
	ds_read_b64_tr_b16 v[136:137], v112 offset:40960
	ds_read_b64_tr_b16 v[138:139], v113 offset:40960
	global_load_dword v115, v88, s[8:9] offset:80
	s_waitcnt lgkmcnt(0)
	v_mfma_f32_32x32x16_bf16 v[0:15], v[132:135], v[136:139], v[0:15]
	ds_read_b128 v[132:135], v129 offset:11264
	ds_read_b64_tr_b16 v[136:137], v112 offset:45056
	ds_read_b64_tr_b16 v[138:139], v113 offset:45056
	global_load_dword v122, v88, s[8:9] offset:88
	s_waitcnt lgkmcnt(0)
	v_mfma_f32_32x32x16_bf16 v[0:15], v[132:135], v[136:139], v[0:15]
	ds_read_b128 v[132:135], v129 offset:12288
	ds_read_b64_tr_b16 v[136:137], v112 offset:49152
	ds_read_b64_tr_b16 v[138:139], v113 offset:49152
	global_load_dword v126, v88, s[8:9] offset:96
	s_waitcnt lgkmcnt(0)
	v_mfma_f32_32x32x16_bf16 v[0:15], v[132:135], v[136:139], v[0:15]
	ds_read_b128 v[132:135], v129 offset:13312
	ds_read_b64_tr_b16 v[136:137], v112 offset:53248
	ds_read_b64_tr_b16 v[138:139], v113 offset:53248
	global_load_dword v127, v88, s[8:9] offset:104
	s_waitcnt lgkmcnt(0)
	v_mfma_f32_32x32x16_bf16 v[0:15], v[132:135], v[136:139], v[0:15]
	ds_read_b128 v[132:135], v129 offset:14336
	ds_read_b64_tr_b16 v[136:137], v112 offset:57344
	ds_read_b64_tr_b16 v[138:139], v113 offset:57344
	global_load_dword v128, v88, s[8:9] offset:112
	s_waitcnt lgkmcnt(0)
	v_mfma_f32_32x32x16_bf16 v[0:15], v[132:135], v[136:139], v[0:15]
	ds_read_b128 v[132:135], v129 offset:15360
	ds_read_b64_tr_b16 v[136:137], v112 offset:61440
	ds_read_b64_tr_b16 v[138:139], v113 offset:61440
	global_load_dword v129, v88, s[8:9] offset:120
	s_movk_i32 s8, 0x100
	v_cmp_gt_i32_e32 vcc, s8, v131
	s_waitcnt lgkmcnt(0)
	v_mfma_f32_32x32x16_bf16 v[0:15], v[132:135], v[136:139], v[0:15]
	s_and_saveexec_b64 s[8:9], vcc
	s_cbranch_execz .LBB0_803
	s_lshl_b64 s[12:13], s[44:45], 2
	s_add_u32 s10, s10, s12
	s_addc_u32 s11, s11, s13
	v_lshlrev_b32_e32 v89, 2, v89
	global_load_dword v91, v89, s[10:11]
	s_branch .LBB0_803
